# v9 with 116 converter workgroups
# speedup vs baseline: 1.0004x; 1.0004x over previous
.LBB0_226:
	s_cmp_lt_i32 s28, 3
	s_cselect_b64 s[0:1], -1, 0
	s_cmp_gt_i32 s29, 2
	s_cselect_b64 s[6:7], -1, 0
	s_and_b64 s[0:1], s[0:1], s[6:7]
	s_andn2_b64 vcc, exec, s[0:1]
	s_cbranch_vccnz .LBB0_398
	s_cmpk_lg_i32 s33, 0x100
	s_cselect_b32 s3, s33, 0x74
	s_sub_i32 s6, s33, s3
	s_cmp_lt_i32 s2, s6
	s_cselect_b64 s[0:1], -1, 0
	s_sub_i32 s30, s2, s6
	s_cmpk_gt_i32 s30, 0x2fff
	s_cselect_b64 s[6:7], -1, 0
	s_or_b64 s[0:1], s[0:1], s[6:7]
	v_lshrrev_b32_e32 v82, 5, v0
	v_lshlrev_b32_e32 v80, 4, v0
	v_lshrrev_b32_e32 v1, 7, v0
	v_lshrrev_b32_e32 v81, 3, v0
	s_and_b64 vcc, exec, s[0:1]
	s_cbranch_vccnz .LBB0_237
	v_readlane_b32 s6, v252, 0
	v_readlane_b32 s7, v252, 1
	v_readfirstlane_b32 s34, v0
	s_nop 4
	s_sub_u32 s6, s6, 0xe8
	s_subb_u32 s7, s7, 0
	s_load_dwordx2 s[8:9], s[6:7], 0xa8
	s_load_dwordx2 s[10:11], s[6:7], 0xb8
	s_lshr_b32 s34, s34, 6
	s_add_u32 s12, s26, 0x5800000
	s_addc_u32 s13, s27, 0
	s_add_u32 s14, s26, 0x25800000
	s_addc_u32 s15, s27, 0
	s_mov_b32 s35, 0xc3e00000
	v_mov_b32_e32 v160, 0x43e00000
	s_mov_b32 s31, 116
	s_sub_u32 s0, 0x2fff, s30
	s_mul_hi_u32 s41, s0, 0x234f72d
	s_add_u32 s41, s41, 1
	v_and_b32_e32 v77, 63, v0
	v_and_b32_e32 v66, 31, v77
	v_lshlrev_b32_e32 v66, 4, v66
	v_lshrrev_b32_e32 v67, 5, v77
	v_lshlrev_b32_e32 v68, 4, v77
	v_lshl_add_u32 v69, v67, 9, v66
	s_lshr_b32 s0, s34, 1
	v_and_b32_e32 v78, 3, v77
	v_xor_b32_e32 v78, s0, v78
	v_and_b32_e32 v71, 4, v77
	v_or_b32_e32 v78, v78, v71
	v_lshlrev_b32_e32 v78, 4, v78
	s_and_b32 s0, s34, 1
	s_lshl_b32 s0, s0, 3
	v_lshl_or_b32 v71, v77, 9, s0
	v_or_b32_e32 v71, v71, v78
	v_xor_b32_e32 v72, 64, v71
	v_add_u32_e32 v73, 0x8000, v71
	v_add_u32_e32 v74, 0x8000, v72
	s_lshl_b32 s0, s34, 1
	v_add_u32_e32 v78, s0, v67
	v_xor_b32_e32 v78, v78, v77
	v_and_b32_e32 v78, 7, v78
	v_lshlrev_b32_e32 v78, 4, v78
	v_lshrrev_b32_e32 v75, 3, v77
	s_lshl_b32 s0, s34, 3
	v_add_u32_e32 v75, s0, v75
	v_and_b32_e32 v76, 7, v77
	v_lshlrev_b32_e32 v76, 4, v76
	v_lshl_add_u32 v76, v75, 11, v76
	v_lshl_add_u32 v75, v75, 7, v78
	s_waitcnt lgkmcnt(0)
	s_min_u32 s0, s30, 0x2fff
	s_add_u32 s30, s30, s31
	s_cmp_lt_u32 s0, 0x2000
	s_cbranch_scc0 .Lcv_w2_1
	s_lshr_b32 s1, s0, 8
	s_bfe_u32 s3, s0, 0x40004
	s_bfe_u32 s7, s0, 0x30001
	s_and_b32 s0, s0, 1
	s_lshl_b32 s6, s1, 25
	s_lshl_b32 s49, s3, 21
	s_add_u32 s6, s6, s49
	s_lshl_b32 s49, s34, 17
	s_add_u32 s6, s6, s49
	s_lshl_b32 s49, s0, 13
	s_add_u32 s6, s6, s49
	s_lshl_b32 s49, s7, 10
	s_add_u32 s6, s6, s49
	s_add_u32 s62, s8, s6
	s_addc_u32 s63, s9, 0
	s_lshl_b32 s6, s1, 23
	s_lshl_b32 s49, s7, 20
	s_add_u32 s6, s6, s49
	s_lshl_b32 s49, s0, 18
	s_add_u32 s6, s6, s49
	s_lshl_b32 s49, s3, 7
	s_add_u32 s6, s6, s49
	s_add_u32 s52, s12, s6
	s_addc_u32 s53, s13, 0
	s_mov_b32 s70, 0x4000
	s_mov_b32 s71, 0xe4000
	s_mov_b32 s86, 0x60000
	v_mov_b32_e32 v70, v68
	s_branch .Lcv_dec_done_1
